# MoBA tile loops: tile(i+2) LDS-DMA pair issued behind the first four K-fragment ds_reads (and on the skip path) instead of right after the barrier
# speedup vs baseline: 1.0157x; 1.0157x over previous
.LBB0_485:
	s_add_i32 s32, s51, 2
	s_cmp_ge_u32 s32, s57
	s_cbranch_scc1 .Lmoba0_b
	s_add_i32 s32, s18, s50
	s_mov_b32 m0, s32
	s_nop 0
	global_load_lds_dwordx4 v[156:157], off
	s_add_i32 m0, s32, 0x6000
	s_nop 0
	global_load_lds_dwordx4 v[158:159], off

.LBB0_487:
	s_waitcnt vmcnt(2) lgkmcnt(0)
	s_barrier
.LBB0_489:
	s_lshr_b32 s52, s51, 2
	s_cmp_eq_u32 s52, s30
	s_cselect_b64 s[0:1], -1, 0
	s_cmp_lg_u32 s52, s30
	s_mov_b64 s[46:47], -1
	s_cbranch_scc0 .LBB0_491
	v_bfe_u32 v32, v198, s52, 1
	v_cmp_ne_u32_e32 vcc, 0, v32
	s_cmp_lg_u64 vcc, 0
	s_mov_b64 s[46:47], 0
	s_cselect_b64 s[6:7], -1, 0

.LBB0_493:
	s_andn2_b64 vcc, exec, s[6:7]
	s_andn2_b64 s[6:7], s[44:45], exec
	s_and_b64 s[46:47], s[44:45], exec
	s_or_b64 s[46:47], s[6:7], s[46:47]
	s_cbranch_vccnz .LBB0_485
	v_add_u32_e32 v32, s56, v199
	v_cvt_f32_i32_e32 v32, v32
	v_add_u32_e32 v160, s33, v165
	s_lshl_b32 s6, 1, s52
	ds_read_b128 v[80:83], v160
	ds_read_b128 v[84:87], v160 offset:512
	ds_read_b128 v[88:91], v160 offset:2048
	ds_read_b128 v[96:99], v160 offset:2560
	s_add_i32 s32, s51, 2
	s_cmp_ge_u32 s32, s57
	s_cbranch_scc1 .Lmoba0_a
	s_add_i32 s32, s18, s50
	s_mov_b32 m0, s32
	s_nop 0
	global_load_lds_dwordx4 v[156:157], off
	s_add_i32 m0, s32, 0x6000
	s_nop 0
	global_load_lds_dwordx4 v[158:159], off
.Lmoba0_a:
	v_and_b32_e32 v33, s6, v198
	v_cmp_ne_u32_e32 vcc, 0, v33
	v_fma_f32 v32, v137, v32, -v197
	s_or_b64 vcc, s[0:1], vcc
	v_cndmask_b32_e32 v32, v192, v32, vcc
	v_pk_add_f32 v[48:49], v[136:137], v[32:33] op_sel_hi:[1,0]
	v_pk_add_f32 v[50:51], v[142:143], v[32:33] op_sel_hi:[1,0]
	v_pk_add_f32 v[52:53], v[144:145], v[32:33] op_sel_hi:[1,0]
	v_pk_add_f32 v[54:55], v[146:147], v[32:33] op_sel_hi:[1,0]
	v_pk_add_f32 v[56:57], v[148:149], v[32:33] op_sel_hi:[1,0]
	v_pk_add_f32 v[58:59], v[150:151], v[32:33] op_sel_hi:[1,0]
	v_pk_add_f32 v[60:61], v[152:153], v[32:33] op_sel_hi:[1,0]
	v_pk_add_f32 v[62:63], v[154:155], v[32:33] op_sel_hi:[1,0]
	v_mov_b32_e32 v139, v138
	v_pk_add_f32 v[46:47], v[138:139], v[62:63]
	v_pk_add_f32 v[44:45], v[138:139], v[60:61]
	v_pk_add_f32 v[42:43], v[138:139], v[58:59]
	v_pk_add_f32 v[40:41], v[138:139], v[56:57]
	v_pk_add_f32 v[38:39], v[138:139], v[54:55]
	v_pk_add_f32 v[36:37], v[138:139], v[52:53]
	v_pk_add_f32 v[34:35], v[138:139], v[50:51]
	v_pk_add_f32 v[32:33], v[140:141], v[48:49]
	v_add_u32_e32 v139, s33, v166
	ds_read_b64_tr_b16 v[100:101], v139 offset:24576
	ds_read_b64_tr_b16 v[102:103], v139 offset:25088
	ds_read_b64_tr_b16 v[92:93], v139 offset:25600
	ds_read_b64_tr_b16 v[94:95], v139 offset:26112
	ds_read_b128 v[104:107], v160 offset:4096
	ds_read_b128 v[108:111], v160 offset:4608
	s_waitcnt lgkmcnt(0)
	v_mfma_f32_32x32x16_bf16 v[48:63], v[80:83], v[76:79], v[48:63]
	v_mfma_f32_32x32x16_bf16 v[32:47], v[84:87], v[76:79], v[32:47]
	ds_read_b64_tr_b16 v[84:85], v139 offset:26624
	ds_read_b64_tr_b16 v[86:87], v139 offset:27136
	ds_read_b64_tr_b16 v[80:81], v139 offset:27648
	ds_read_b64_tr_b16 v[82:83], v139 offset:28160
	ds_read_b128 v[202:205], v160 offset:6144
	ds_read_b128 v[206:209], v160 offset:6656
	v_mfma_f32_32x32x16_bf16 v[48:63], v[88:91], v[72:75], v[48:63]
	v_mfma_f32_32x32x16_bf16 v[32:47], v[96:99], v[72:75], v[32:47]
	v_mfma_f32_32x32x16_bf16 v[48:63], v[104:107], v[68:71], v[48:63]
	v_mfma_f32_32x32x16_bf16 v[32:47], v[108:111], v[68:71], v[32:47]
	s_waitcnt lgkmcnt(0)
	v_mfma_f32_32x32x16_bf16 v[48:63], v[202:205], v[64:67], v[48:63]
	ds_read_b64_tr_b16 v[108:109], v139 offset:28672
	ds_read_b64_tr_b16 v[110:111], v139 offset:29184
	ds_read_b64_tr_b16 v[104:105], v139 offset:29696
	ds_read_b64_tr_b16 v[106:107], v139 offset:30208
	v_mfma_f32_32x32x16_bf16 v[32:47], v[206:209], v[64:67], v[32:47]
	ds_read_b64_tr_b16 v[96:97], v139 offset:30720
	ds_read_b64_tr_b16 v[98:99], v139 offset:31232
	ds_read_b64_tr_b16 v[88:89], v139 offset:31744
	ds_read_b64_tr_b16 v[90:91], v139 offset:32256
	s_add_i32 s6, s56, 63
	s_cmp_gt_u32 s6, s8
	s_cselect_b64 s[6:7], -1, 0
	s_and_b64 s[0:1], s[0:1], s[6:7]
	s_andn2_b64 vcc, exec, s[0:1]
	s_cbranch_vccnz .LBB0_496
	v_add_u32_e32 v139, 27, v200
	v_cmp_lt_i32_e32 vcc, -1, v139
	s_nop 1
	v_cndmask_b32_e32 v48, v192, v48, vcc
	v_cmp_lt_i32_e32 vcc, 31, v139
	v_add_u32_e32 v139, 26, v200
	s_nop 0
	v_cndmask_b32_e32 v32, v192, v32, vcc
	v_cmp_lt_i32_e32 vcc, -1, v139
	s_nop 1
	v_cndmask_b32_e32 v49, v192, v49, vcc
	v_cmp_lt_i32_e32 vcc, 31, v139
	v_add_u32_e32 v139, 25, v200
	s_nop 0
	v_cndmask_b32_e32 v33, v192, v33, vcc
	v_cmp_lt_i32_e32 vcc, -1, v139
	s_nop 1
	v_cndmask_b32_e32 v50, v192, v50, vcc
	v_cmp_lt_i32_e32 vcc, 31, v139
	v_add_u32_e32 v139, 24, v200
	s_nop 0
	v_cndmask_b32_e32 v34, v192, v34, vcc
	v_cmp_lt_i32_e32 vcc, -1, v139
	s_nop 1
	v_cndmask_b32_e32 v51, v192, v51, vcc
	v_cmp_lt_i32_e32 vcc, 31, v139
	v_add_u32_e32 v139, 19, v200
	s_nop 0
	v_cndmask_b32_e32 v35, v192, v35, vcc
	v_cmp_lt_i32_e32 vcc, -1, v139
	s_nop 1
	v_cndmask_b32_e32 v52, v192, v52, vcc
	v_cmp_lt_i32_e32 vcc, 31, v139
	v_add_u32_e32 v139, 18, v200
	s_nop 0
	v_cndmask_b32_e32 v36, v192, v36, vcc
	v_cmp_lt_i32_e32 vcc, -1, v139
	s_nop 1
	v_cndmask_b32_e32 v53, v192, v53, vcc
	v_cmp_lt_i32_e32 vcc, 31, v139
	v_add_u32_e32 v139, 17, v200
	s_nop 0
	v_cndmask_b32_e32 v37, v192, v37, vcc
	v_cmp_lt_i32_e32 vcc, -1, v139
	s_nop 1
	v_cndmask_b32_e32 v54, v192, v54, vcc
	v_cmp_lt_i32_e32 vcc, 31, v139
	v_add_u32_e32 v139, 16, v200
	s_nop 0
	v_cndmask_b32_e32 v38, v192, v38, vcc
	v_cmp_lt_i32_e32 vcc, -1, v139
	s_nop 1
	v_cndmask_b32_e32 v55, v192, v55, vcc
	v_cmp_lt_i32_e32 vcc, 31, v139
	v_add_u32_e32 v139, 11, v200
	s_nop 0
	v_cndmask_b32_e32 v39, v192, v39, vcc
	v_cmp_lt_i32_e32 vcc, -1, v139
	s_nop 1
	v_cndmask_b32_e32 v56, v192, v56, vcc
	v_cmp_lt_i32_e32 vcc, 31, v139
	v_add_u32_e32 v139, 10, v200
	s_nop 0
	v_cndmask_b32_e32 v40, v192, v40, vcc
	v_cmp_lt_i32_e32 vcc, -1, v139
	s_nop 1
	v_cndmask_b32_e32 v57, v192, v57, vcc
	v_cmp_lt_i32_e32 vcc, 31, v139
	v_add_u32_e32 v139, 9, v200
	s_nop 0
	v_cndmask_b32_e32 v41, v192, v41, vcc
	v_cmp_lt_i32_e32 vcc, -1, v139
	s_nop 1
	v_cndmask_b32_e32 v58, v192, v58, vcc
	v_cmp_lt_i32_e32 vcc, 31, v139
	v_add_u32_e32 v139, 8, v200
	s_nop 0
	v_cndmask_b32_e32 v42, v192, v42, vcc
	v_cmp_lt_i32_e32 vcc, -1, v139
	s_nop 1
	v_cndmask_b32_e32 v59, v192, v59, vcc
	v_cmp_lt_i32_e32 vcc, 31, v139
	v_add_u32_e32 v139, 3, v200
	s_nop 0
	v_cndmask_b32_e32 v43, v192, v43, vcc
	v_cmp_lt_i32_e32 vcc, -1, v139
	s_nop 1
	v_cndmask_b32_e32 v60, v192, v60, vcc
	v_cmp_lt_i32_e32 vcc, 31, v139
	v_add_u32_e32 v139, 2, v200
	s_nop 0
	v_cndmask_b32_e32 v44, v192, v44, vcc
	v_cmp_lt_i32_e32 vcc, -1, v139
	s_nop 1
	v_cndmask_b32_e32 v61, v192, v61, vcc
	v_cmp_lt_i32_e32 vcc, 31, v139
	v_add_u32_e32 v139, 1, v200
	s_nop 0
	v_cndmask_b32_e32 v45, v192, v45, vcc
	v_cmp_lt_i32_e32 vcc, -1, v139
	s_nop 1
	v_cndmask_b32_e32 v62, v192, v62, vcc
	v_cmp_lt_i32_e32 vcc, 31, v139
	s_nop 1
	v_cndmask_b32_e32 v46, v192, v46, vcc
	v_cmp_lt_i32_e32 vcc, -1, v200
	s_nop 1
	v_cndmask_b32_e32 v63, v192, v63, vcc
	v_cmp_lt_i32_e32 vcc, 31, v200
	s_nop 1
	v_cndmask_b32_e32 v47, v192, v47, vcc

.LBB0_3024:
	s_add_i32 s32, s40, 2
	s_cmp_ge_u32 s32, s57
	s_cbranch_scc1 .Lmoba1_b
	s_add_i32 s32, s43, s39
	s_mov_b32 m0, s32
	s_nop 0
	global_load_lds_dwordx4 v[156:157], off
	s_add_i32 m0, s32, 0x6000
	s_nop 0
	global_load_lds_dwordx4 v[158:159], off

.LBB0_3026:
	s_waitcnt vmcnt(2) lgkmcnt(0)
	s_barrier
.LBB0_3028:
	s_lshr_b32 s41, s40, 2
	s_cmp_eq_u32 s41, s52
	s_cselect_b64 s[0:1], -1, 0
	s_cmp_lg_u32 s41, s52
	s_mov_b64 s[34:35], -1
	s_cbranch_scc0 .LBB0_3030
	v_bfe_u32 v32, v198, s41, 1
	v_cmp_ne_u32_e32 vcc, 0, v32
	s_cmp_lg_u64 vcc, 0
	s_mov_b64 s[34:35], 0
	s_cselect_b64 s[6:7], -1, 0

.LBB0_3032:
	s_andn2_b64 vcc, exec, s[6:7]
	s_andn2_b64 s[6:7], s[30:31], exec
	s_and_b64 s[34:35], s[30:31], exec
	s_or_b64 s[34:35], s[6:7], s[34:35]
	s_cbranch_vccnz .LBB0_3024
	v_add_u32_e32 v32, s56, v199
	v_cvt_f32_i32_e32 v32, v32
	v_add_u32_e32 v160, s36, v165
	s_lshl_b32 s6, 1, s41
	ds_read_b128 v[80:83], v160
	ds_read_b128 v[88:91], v160 offset:512
	ds_read_b128 v[96:99], v160 offset:2048
	ds_read_b128 v[104:107], v160 offset:2560
	s_add_i32 s32, s40, 2
	s_cmp_ge_u32 s32, s57
	s_cbranch_scc1 .Lmoba1_a
	s_add_i32 s32, s43, s39
	s_mov_b32 m0, s32
	s_nop 0
	global_load_lds_dwordx4 v[156:157], off
	s_add_i32 m0, s32, 0x6000
	s_nop 0
	global_load_lds_dwordx4 v[158:159], off
.Lmoba1_a:
	v_and_b32_e32 v33, s6, v198
	v_cmp_ne_u32_e32 vcc, 0, v33
	v_fma_f32 v32, v137, v32, -v197
	s_or_b64 vcc, s[0:1], vcc
	v_cndmask_b32_e32 v32, v192, v32, vcc
	v_pk_add_f32 v[48:49], v[136:137], v[32:33] op_sel_hi:[1,0]
	v_pk_add_f32 v[50:51], v[142:143], v[32:33] op_sel_hi:[1,0]
	v_pk_add_f32 v[52:53], v[144:145], v[32:33] op_sel_hi:[1,0]
	v_pk_add_f32 v[54:55], v[146:147], v[32:33] op_sel_hi:[1,0]
	v_pk_add_f32 v[56:57], v[148:149], v[32:33] op_sel_hi:[1,0]
	v_pk_add_f32 v[58:59], v[150:151], v[32:33] op_sel_hi:[1,0]
	v_pk_add_f32 v[60:61], v[152:153], v[32:33] op_sel_hi:[1,0]
	v_pk_add_f32 v[62:63], v[154:155], v[32:33] op_sel_hi:[1,0]
	v_mov_b32_e32 v139, v138
	v_pk_add_f32 v[46:47], v[138:139], v[62:63]
	v_pk_add_f32 v[44:45], v[138:139], v[60:61]
	v_pk_add_f32 v[42:43], v[138:139], v[58:59]
	v_pk_add_f32 v[40:41], v[138:139], v[56:57]
	v_pk_add_f32 v[38:39], v[138:139], v[54:55]
	v_pk_add_f32 v[36:37], v[138:139], v[52:53]
	v_pk_add_f32 v[34:35], v[138:139], v[50:51]
	v_pk_add_f32 v[32:33], v[140:141], v[48:49]
	v_add_u32_e32 v139, s36, v166
	ds_read_b64_tr_b16 v[100:101], v139 offset:24576
	ds_read_b64_tr_b16 v[102:103], v139 offset:25088
	ds_read_b64_tr_b16 v[92:93], v139 offset:25600
	ds_read_b64_tr_b16 v[94:95], v139 offset:26112
	ds_read_b128 v[108:111], v160 offset:4096
	ds_read_b128 v[202:205], v160 offset:4608
	s_waitcnt lgkmcnt(0)
	v_mfma_f32_32x32x16_bf16 v[48:63], v[80:83], v[76:79], v[48:63]
	ds_read_b64_tr_b16 v[84:85], v139 offset:26624
	ds_read_b64_tr_b16 v[86:87], v139 offset:27136
	ds_read_b64_tr_b16 v[80:81], v139 offset:27648
	ds_read_b64_tr_b16 v[82:83], v139 offset:28160
	ds_read_b128 v[206:209], v160 offset:6144
	ds_read_b128 v[210:213], v160 offset:6656
	v_mfma_f32_32x32x16_bf16 v[32:47], v[88:91], v[76:79], v[32:47]
	v_mfma_f32_32x32x16_bf16 v[48:63], v[96:99], v[72:75], v[48:63]
	v_mfma_f32_32x32x16_bf16 v[32:47], v[104:107], v[72:75], v[32:47]
	v_mfma_f32_32x32x16_bf16 v[48:63], v[108:111], v[68:71], v[48:63]
	v_mfma_f32_32x32x16_bf16 v[32:47], v[202:205], v[68:71], v[32:47]
	s_waitcnt lgkmcnt(0)
	v_mfma_f32_32x32x16_bf16 v[48:63], v[206:209], v[64:67], v[48:63]
	ds_read_b64_tr_b16 v[108:109], v139 offset:28672
	ds_read_b64_tr_b16 v[110:111], v139 offset:29184
	ds_read_b64_tr_b16 v[104:105], v139 offset:29696
	ds_read_b64_tr_b16 v[106:107], v139 offset:30208
	v_mfma_f32_32x32x16_bf16 v[32:47], v[210:213], v[64:67], v[32:47]
	ds_read_b64_tr_b16 v[96:97], v139 offset:30720
	ds_read_b64_tr_b16 v[98:99], v139 offset:31232
	ds_read_b64_tr_b16 v[88:89], v139 offset:31744
	ds_read_b64_tr_b16 v[90:91], v139 offset:32256
	s_add_i32 s6, s56, 63
	s_cmp_gt_u32 s6, s8
	s_cselect_b64 s[6:7], -1, 0
	s_and_b64 s[0:1], s[0:1], s[6:7]
	s_andn2_b64 vcc, exec, s[0:1]
	s_cbranch_vccnz .LBB0_3035
	v_add_u32_e32 v139, 27, v200
	v_cmp_lt_i32_e32 vcc, -1, v139
	s_nop 1
	v_cndmask_b32_e32 v48, v192, v48, vcc
	v_cmp_lt_i32_e32 vcc, 31, v139
	v_add_u32_e32 v139, 26, v200
	s_nop 0
	v_cndmask_b32_e32 v32, v192, v32, vcc
	v_cmp_lt_i32_e32 vcc, -1, v139
	s_nop 1
	v_cndmask_b32_e32 v49, v192, v49, vcc
	v_cmp_lt_i32_e32 vcc, 31, v139
	v_add_u32_e32 v139, 25, v200
	s_nop 0
	v_cndmask_b32_e32 v33, v192, v33, vcc
	v_cmp_lt_i32_e32 vcc, -1, v139
	s_nop 1
	v_cndmask_b32_e32 v50, v192, v50, vcc
	v_cmp_lt_i32_e32 vcc, 31, v139
	v_add_u32_e32 v139, 24, v200
	s_nop 0
	v_cndmask_b32_e32 v34, v192, v34, vcc
	v_cmp_lt_i32_e32 vcc, -1, v139
	s_nop 1
	v_cndmask_b32_e32 v51, v192, v51, vcc
	v_cmp_lt_i32_e32 vcc, 31, v139
	v_add_u32_e32 v139, 19, v200
	s_nop 0
	v_cndmask_b32_e32 v35, v192, v35, vcc
	v_cmp_lt_i32_e32 vcc, -1, v139
	s_nop 1
	v_cndmask_b32_e32 v52, v192, v52, vcc
	v_cmp_lt_i32_e32 vcc, 31, v139
	v_add_u32_e32 v139, 18, v200
	s_nop 0
	v_cndmask_b32_e32 v36, v192, v36, vcc
	v_cmp_lt_i32_e32 vcc, -1, v139
	s_nop 1
	v_cndmask_b32_e32 v53, v192, v53, vcc
	v_cmp_lt_i32_e32 vcc, 31, v139
	v_add_u32_e32 v139, 17, v200
	s_nop 0
	v_cndmask_b32_e32 v37, v192, v37, vcc
	v_cmp_lt_i32_e32 vcc, -1, v139
	s_nop 1
	v_cndmask_b32_e32 v54, v192, v54, vcc
	v_cmp_lt_i32_e32 vcc, 31, v139
	v_add_u32_e32 v139, 16, v200
	s_nop 0
	v_cndmask_b32_e32 v38, v192, v38, vcc
	v_cmp_lt_i32_e32 vcc, -1, v139
	s_nop 1
	v_cndmask_b32_e32 v55, v192, v55, vcc
	v_cmp_lt_i32_e32 vcc, 31, v139
	v_add_u32_e32 v139, 11, v200
	s_nop 0
	v_cndmask_b32_e32 v39, v192, v39, vcc
	v_cmp_lt_i32_e32 vcc, -1, v139
	s_nop 1
	v_cndmask_b32_e32 v56, v192, v56, vcc
	v_cmp_lt_i32_e32 vcc, 31, v139
	v_add_u32_e32 v139, 10, v200
	s_nop 0
	v_cndmask_b32_e32 v40, v192, v40, vcc
	v_cmp_lt_i32_e32 vcc, -1, v139
	s_nop 1
	v_cndmask_b32_e32 v57, v192, v57, vcc
	v_cmp_lt_i32_e32 vcc, 31, v139
	v_add_u32_e32 v139, 9, v200
	s_nop 0
	v_cndmask_b32_e32 v41, v192, v41, vcc
	v_cmp_lt_i32_e32 vcc, -1, v139
	s_nop 1
	v_cndmask_b32_e32 v58, v192, v58, vcc
	v_cmp_lt_i32_e32 vcc, 31, v139
	v_add_u32_e32 v139, 8, v200
	s_nop 0
	v_cndmask_b32_e32 v42, v192, v42, vcc
	v_cmp_lt_i32_e32 vcc, -1, v139
	s_nop 1
	v_cndmask_b32_e32 v59, v192, v59, vcc
	v_cmp_lt_i32_e32 vcc, 31, v139
	v_add_u32_e32 v139, 3, v200
	s_nop 0
	v_cndmask_b32_e32 v43, v192, v43, vcc
	v_cmp_lt_i32_e32 vcc, -1, v139
	s_nop 1
	v_cndmask_b32_e32 v60, v192, v60, vcc
	v_cmp_lt_i32_e32 vcc, 31, v139
	v_add_u32_e32 v139, 2, v200
	s_nop 0
	v_cndmask_b32_e32 v44, v192, v44, vcc
	v_cmp_lt_i32_e32 vcc, -1, v139
	s_nop 1
	v_cndmask_b32_e32 v61, v192, v61, vcc
	v_cmp_lt_i32_e32 vcc, 31, v139
	v_add_u32_e32 v139, 1, v200
	s_nop 0
	v_cndmask_b32_e32 v45, v192, v45, vcc
	v_cmp_lt_i32_e32 vcc, -1, v139
	s_nop 1
	v_cndmask_b32_e32 v62, v192, v62, vcc
	v_cmp_lt_i32_e32 vcc, 31, v139
	s_nop 1
	v_cndmask_b32_e32 v46, v192, v46, vcc
	v_cmp_lt_i32_e32 vcc, -1, v200
	s_nop 1
	v_cndmask_b32_e32 v63, v192, v63, vcc
	v_cmp_lt_i32_e32 vcc, 31, v200
	s_nop 1
	v_cndmask_b32_e32 v47, v192, v47, vcc
